# indexer radix select: 5-instruction histogram accumulate per key (no compare/select chain)
# speedup vs baseline: 1.0004x; 1.0004x over previous
.LBB0_971:
	s_mov_b32 s48, s49
	s_cmp_eq_u32 s33, 24
	s_mov_b32 s50, s49
	s_mov_b32 s51, s49
	v_mov_b64_e32 v[4:5], s[48:49]
	s_cselect_b64 s[18:19], -1, 0
	s_sub_i32 s4, s33, 24
	v_mov_b64_e32 v[6:7], s[50:51]
	s_and_b32 s4, s4, 24
	ds_write_b128 v28, v[4:7]
	ds_write_b128 v28, v[4:7] offset:16
	ds_write_b128 v28, v[4:7] offset:32
	ds_write_b128 v28, v[4:7] offset:48
	ds_write_b32 v55, v3 offset:1024
	s_andn2_b64 vcc, exec, s[20:21]
	v_lshrrev_b32_e32 v4, s4, v22
	v_lshlrev_b32_e32 v0, 8, v4
	s_cbranch_vccnz .LBB0_973
	v_lshrrev_b32_e32 v5, s33, v78
	v_sub_u32_e32 v5, v5, v0
	v_min_u32_e32 v5, v5, v26
	v_lshl_add_u32 v5, v5, 2, v27
	ds_add_u32 v5, v232
	v_lshrrev_b32_e32 v5, s33, v77
	v_sub_u32_e32 v5, v5, v0
	v_min_u32_e32 v5, v5, v26
	v_lshl_add_u32 v5, v5, 2, v27
	ds_add_u32 v5, v232
	v_lshrrev_b32_e32 v5, s33, v80
	v_sub_u32_e32 v5, v5, v0
	v_min_u32_e32 v5, v5, v26
	v_lshl_add_u32 v5, v5, 2, v27
	ds_add_u32 v5, v232
	v_lshrrev_b32_e32 v5, s33, v79
	v_sub_u32_e32 v5, v5, v0
	v_min_u32_e32 v5, v5, v26
	v_lshl_add_u32 v5, v5, 2, v27
	ds_add_u32 v5, v232
	v_lshrrev_b32_e32 v5, s33, v82
	v_sub_u32_e32 v5, v5, v0
	v_min_u32_e32 v5, v5, v26
	v_lshl_add_u32 v5, v5, 2, v27
	ds_add_u32 v5, v232
	v_lshrrev_b32_e32 v5, s33, v81
	v_sub_u32_e32 v5, v5, v0
	v_min_u32_e32 v5, v5, v26
	v_lshl_add_u32 v5, v5, 2, v27
	ds_add_u32 v5, v232
	v_lshrrev_b32_e32 v5, s33, v84
	v_sub_u32_e32 v5, v5, v0
	v_min_u32_e32 v5, v5, v26
	v_lshl_add_u32 v5, v5, 2, v27
	ds_add_u32 v5, v232
	v_lshrrev_b32_e32 v5, s33, v83
	v_sub_u32_e32 v5, v5, v0
	v_min_u32_e32 v5, v5, v26
	v_lshl_add_u32 v5, v5, 2, v27
	ds_add_u32 v5, v232
	v_lshrrev_b32_e32 v5, s33, v86
	v_sub_u32_e32 v5, v5, v0
	v_min_u32_e32 v5, v5, v26
	v_lshl_add_u32 v5, v5, 2, v27
	ds_add_u32 v5, v232
	v_lshrrev_b32_e32 v5, s33, v85
	v_sub_u32_e32 v5, v5, v0
	v_min_u32_e32 v5, v5, v26
	v_lshl_add_u32 v5, v5, 2, v27
	ds_add_u32 v5, v232
	v_lshrrev_b32_e32 v5, s33, v88
	v_sub_u32_e32 v5, v5, v0
	v_min_u32_e32 v5, v5, v26
	v_lshl_add_u32 v5, v5, 2, v27
	ds_add_u32 v5, v232
	v_lshrrev_b32_e32 v5, s33, v87
	v_sub_u32_e32 v5, v5, v0
	v_min_u32_e32 v5, v5, v26
	v_lshl_add_u32 v5, v5, 2, v27
	ds_add_u32 v5, v232
	v_lshrrev_b32_e32 v5, s33, v90
	v_sub_u32_e32 v5, v5, v0
	v_min_u32_e32 v5, v5, v26
	v_lshl_add_u32 v5, v5, 2, v27
	ds_add_u32 v5, v232
	v_lshrrev_b32_e32 v5, s33, v89
	v_sub_u32_e32 v5, v5, v0
	v_min_u32_e32 v5, v5, v26
	v_lshl_add_u32 v5, v5, 2, v27
	ds_add_u32 v5, v232
	v_lshrrev_b32_e32 v5, s33, v92
	v_sub_u32_e32 v5, v5, v0
	v_min_u32_e32 v5, v5, v26
	v_lshl_add_u32 v5, v5, 2, v27
	ds_add_u32 v5, v232
	v_lshrrev_b32_e32 v5, s33, v91
	v_sub_u32_e32 v5, v5, v0
	v_min_u32_e32 v5, v5, v26
	v_lshl_add_u32 v5, v5, 2, v27
	ds_add_u32 v5, v232
.LBB0_973:
	s_andn2_b64 vcc, exec, s[0:1]
	s_cbranch_vccnz .LBB0_1039
	v_lshrrev_b32_e32 v5, s33, v94
	v_sub_u32_e32 v5, v5, v0
	v_min_u32_e32 v5, v5, v26
	v_lshl_add_u32 v5, v5, 2, v27
	ds_add_u32 v5, v232
	v_lshrrev_b32_e32 v5, s33, v93
	v_sub_u32_e32 v5, v5, v0
	v_min_u32_e32 v5, v5, v26
	v_lshl_add_u32 v5, v5, 2, v27
	ds_add_u32 v5, v232
	v_lshrrev_b32_e32 v5, s33, v96
	v_sub_u32_e32 v5, v5, v0
	v_min_u32_e32 v5, v5, v26
	v_lshl_add_u32 v5, v5, 2, v27
	ds_add_u32 v5, v232
	v_lshrrev_b32_e32 v5, s33, v95
	v_sub_u32_e32 v5, v5, v0
	v_min_u32_e32 v5, v5, v26
	v_lshl_add_u32 v5, v5, 2, v27
	ds_add_u32 v5, v232
	v_lshrrev_b32_e32 v5, s33, v98
	v_sub_u32_e32 v5, v5, v0
	v_min_u32_e32 v5, v5, v26
	v_lshl_add_u32 v5, v5, 2, v27
	ds_add_u32 v5, v232
	v_lshrrev_b32_e32 v5, s33, v97
	v_sub_u32_e32 v5, v5, v0
	v_min_u32_e32 v5, v5, v26
	v_lshl_add_u32 v5, v5, 2, v27
	ds_add_u32 v5, v232
	v_lshrrev_b32_e32 v5, s33, v100
	v_sub_u32_e32 v5, v5, v0
	v_min_u32_e32 v5, v5, v26
	v_lshl_add_u32 v5, v5, 2, v27
	ds_add_u32 v5, v232
	v_lshrrev_b32_e32 v5, s33, v99
	v_sub_u32_e32 v5, v5, v0
	v_min_u32_e32 v5, v5, v26
	v_lshl_add_u32 v5, v5, 2, v27
	ds_add_u32 v5, v232
	v_lshrrev_b32_e32 v5, s33, v102
	v_sub_u32_e32 v5, v5, v0
	v_min_u32_e32 v5, v5, v26
	v_lshl_add_u32 v5, v5, 2, v27
	ds_add_u32 v5, v232
	v_lshrrev_b32_e32 v5, s33, v101
	v_sub_u32_e32 v5, v5, v0
	v_min_u32_e32 v5, v5, v26
	v_lshl_add_u32 v5, v5, 2, v27
	ds_add_u32 v5, v232
	v_lshrrev_b32_e32 v5, s33, v104
	v_sub_u32_e32 v5, v5, v0
	v_min_u32_e32 v5, v5, v26
	v_lshl_add_u32 v5, v5, 2, v27
	ds_add_u32 v5, v232
	v_lshrrev_b32_e32 v5, s33, v103
	v_sub_u32_e32 v5, v5, v0
	v_min_u32_e32 v5, v5, v26
	v_lshl_add_u32 v5, v5, 2, v27
	ds_add_u32 v5, v232
	v_lshrrev_b32_e32 v5, s33, v106
	v_sub_u32_e32 v5, v5, v0
	v_min_u32_e32 v5, v5, v26
	v_lshl_add_u32 v5, v5, 2, v27
	ds_add_u32 v5, v232
	v_lshrrev_b32_e32 v5, s33, v105
	v_sub_u32_e32 v5, v5, v0
	v_min_u32_e32 v5, v5, v26
	v_lshl_add_u32 v5, v5, 2, v27
	ds_add_u32 v5, v232
	v_lshrrev_b32_e32 v5, s33, v108
	v_sub_u32_e32 v5, v5, v0
	v_min_u32_e32 v5, v5, v26
	v_lshl_add_u32 v5, v5, 2, v27
	ds_add_u32 v5, v232
	v_lshrrev_b32_e32 v5, s33, v107
	v_sub_u32_e32 v5, v5, v0
	v_min_u32_e32 v5, v5, v26
	v_lshl_add_u32 v5, v5, 2, v27
	ds_add_u32 v5, v232
	s_andn2_b64 vcc, exec, s[92:93]
	s_cbranch_vccz .LBB0_1040

.LBB0_976:
	v_lshrrev_b32_e32 v5, s33, v126
	v_sub_u32_e32 v5, v5, v0
	v_min_u32_e32 v5, v5, v26
	v_lshl_add_u32 v5, v5, 2, v27
	ds_add_u32 v5, v232
	v_lshrrev_b32_e32 v5, s33, v125
	v_sub_u32_e32 v5, v5, v0
	v_min_u32_e32 v5, v5, v26
	v_lshl_add_u32 v5, v5, 2, v27
	ds_add_u32 v5, v232
	v_lshrrev_b32_e32 v5, s33, v128
	v_sub_u32_e32 v5, v5, v0
	v_min_u32_e32 v5, v5, v26
	v_lshl_add_u32 v5, v5, 2, v27
	ds_add_u32 v5, v232
	v_lshrrev_b32_e32 v5, s33, v127
	v_sub_u32_e32 v5, v5, v0
	v_min_u32_e32 v5, v5, v26
	v_lshl_add_u32 v5, v5, 2, v27
	ds_add_u32 v5, v232
	v_lshrrev_b32_e32 v5, s33, v130
	v_sub_u32_e32 v5, v5, v0
	v_min_u32_e32 v5, v5, v26
	v_lshl_add_u32 v5, v5, 2, v27
	ds_add_u32 v5, v232
	v_lshrrev_b32_e32 v5, s33, v129
	v_sub_u32_e32 v5, v5, v0
	v_min_u32_e32 v5, v5, v26
	v_lshl_add_u32 v5, v5, 2, v27
	ds_add_u32 v5, v232
	v_lshrrev_b32_e32 v5, s33, v132
	v_sub_u32_e32 v5, v5, v0
	v_min_u32_e32 v5, v5, v26
	v_lshl_add_u32 v5, v5, 2, v27
	ds_add_u32 v5, v232
	v_lshrrev_b32_e32 v5, s33, v131
	v_sub_u32_e32 v5, v5, v0
	v_min_u32_e32 v5, v5, v26
	v_lshl_add_u32 v5, v5, 2, v27
	ds_add_u32 v5, v232
	v_lshrrev_b32_e32 v5, s33, v134
	v_sub_u32_e32 v5, v5, v0
	v_min_u32_e32 v5, v5, v26
	v_lshl_add_u32 v5, v5, 2, v27
	ds_add_u32 v5, v232
	v_lshrrev_b32_e32 v5, s33, v133
	v_sub_u32_e32 v5, v5, v0
	v_min_u32_e32 v5, v5, v26
	v_lshl_add_u32 v5, v5, 2, v27
	ds_add_u32 v5, v232
	v_lshrrev_b32_e32 v5, s33, v136
	v_sub_u32_e32 v5, v5, v0
	v_min_u32_e32 v5, v5, v26
	v_lshl_add_u32 v5, v5, 2, v27
	ds_add_u32 v5, v232
	v_lshrrev_b32_e32 v5, s33, v135
	v_sub_u32_e32 v5, v5, v0
	v_min_u32_e32 v5, v5, v26
	v_lshl_add_u32 v5, v5, 2, v27
	ds_add_u32 v5, v232
	v_lshrrev_b32_e32 v5, s33, v138
	v_sub_u32_e32 v5, v5, v0
	v_min_u32_e32 v5, v5, v26
	v_lshl_add_u32 v5, v5, 2, v27
	ds_add_u32 v5, v232
	v_lshrrev_b32_e32 v5, s33, v137
	v_sub_u32_e32 v5, v5, v0
	v_min_u32_e32 v5, v5, v26
	v_lshl_add_u32 v5, v5, 2, v27
	ds_add_u32 v5, v232
	v_lshrrev_b32_e32 v5, s33, v140
	v_sub_u32_e32 v5, v5, v0
	v_min_u32_e32 v5, v5, v26
	v_lshl_add_u32 v5, v5, 2, v27
	ds_add_u32 v5, v232
	v_lshrrev_b32_e32 v5, s33, v139
	v_sub_u32_e32 v5, v5, v0
	v_min_u32_e32 v5, v5, v26
	v_lshl_add_u32 v5, v5, 2, v27
	ds_add_u32 v5, v232
	s_andn2_b64 vcc, exec, s[70:71]
	s_cbranch_vccz .LBB0_1042

.LBB0_978:
	v_lshrrev_b32_e32 v5, s33, v158
	v_sub_u32_e32 v5, v5, v0
	v_min_u32_e32 v5, v5, v26
	v_lshl_add_u32 v5, v5, 2, v27
	ds_add_u32 v5, v232
	v_lshrrev_b32_e32 v5, s33, v157
	v_sub_u32_e32 v5, v5, v0
	v_min_u32_e32 v5, v5, v26
	v_lshl_add_u32 v5, v5, 2, v27
	ds_add_u32 v5, v232
	v_lshrrev_b32_e32 v5, s33, v160
	v_sub_u32_e32 v5, v5, v0
	v_min_u32_e32 v5, v5, v26
	v_lshl_add_u32 v5, v5, 2, v27
	ds_add_u32 v5, v232
	v_lshrrev_b32_e32 v5, s33, v159
	v_sub_u32_e32 v5, v5, v0
	v_min_u32_e32 v5, v5, v26
	v_lshl_add_u32 v5, v5, 2, v27
	ds_add_u32 v5, v232
	v_lshrrev_b32_e32 v5, s33, v162
	v_sub_u32_e32 v5, v5, v0
	v_min_u32_e32 v5, v5, v26
	v_lshl_add_u32 v5, v5, 2, v27
	ds_add_u32 v5, v232
	v_lshrrev_b32_e32 v5, s33, v161
	v_sub_u32_e32 v5, v5, v0
	v_min_u32_e32 v5, v5, v26
	v_lshl_add_u32 v5, v5, 2, v27
	ds_add_u32 v5, v232
	v_lshrrev_b32_e32 v5, s33, v164
	v_sub_u32_e32 v5, v5, v0
	v_min_u32_e32 v5, v5, v26
	v_lshl_add_u32 v5, v5, 2, v27
	ds_add_u32 v5, v232
	v_lshrrev_b32_e32 v5, s33, v163
	v_sub_u32_e32 v5, v5, v0
	v_min_u32_e32 v5, v5, v26
	v_lshl_add_u32 v5, v5, 2, v27
	ds_add_u32 v5, v232
	v_lshrrev_b32_e32 v5, s33, v166
	v_sub_u32_e32 v5, v5, v0
	v_min_u32_e32 v5, v5, v26
	v_lshl_add_u32 v5, v5, 2, v27
	ds_add_u32 v5, v232
	v_lshrrev_b32_e32 v5, s33, v165
	v_sub_u32_e32 v5, v5, v0
	v_min_u32_e32 v5, v5, v26
	v_lshl_add_u32 v5, v5, 2, v27
	ds_add_u32 v5, v232
	v_lshrrev_b32_e32 v5, s33, v168
	v_sub_u32_e32 v5, v5, v0
	v_min_u32_e32 v5, v5, v26
	v_lshl_add_u32 v5, v5, 2, v27
	ds_add_u32 v5, v232
	v_lshrrev_b32_e32 v5, s33, v167
	v_sub_u32_e32 v5, v5, v0
	v_min_u32_e32 v5, v5, v26
	v_lshl_add_u32 v5, v5, 2, v27
	ds_add_u32 v5, v232
	v_lshrrev_b32_e32 v5, s33, v170
	v_sub_u32_e32 v5, v5, v0
	v_min_u32_e32 v5, v5, v26
	v_lshl_add_u32 v5, v5, 2, v27
	ds_add_u32 v5, v232
	v_lshrrev_b32_e32 v5, s33, v169
	v_sub_u32_e32 v5, v5, v0
	v_min_u32_e32 v5, v5, v26
	v_lshl_add_u32 v5, v5, 2, v27
	ds_add_u32 v5, v232
	v_lshrrev_b32_e32 v5, s33, v172
	v_sub_u32_e32 v5, v5, v0
	v_min_u32_e32 v5, v5, v26
	v_lshl_add_u32 v5, v5, 2, v27
	ds_add_u32 v5, v232
	v_lshrrev_b32_e32 v5, s33, v171
	v_sub_u32_e32 v5, v5, v0
	v_min_u32_e32 v5, v5, v26
	v_lshl_add_u32 v5, v5, 2, v27
	ds_add_u32 v5, v232
	s_andn2_b64 vcc, exec, s[56:57]
	s_cbranch_vccz .LBB0_1044

.LBB0_980:
	v_lshrrev_b32_e32 v5, s33, v190
	v_sub_u32_e32 v5, v5, v0
	v_min_u32_e32 v5, v5, v26
	v_lshl_add_u32 v5, v5, 2, v27
	ds_add_u32 v5, v232
	v_lshrrev_b32_e32 v5, s33, v189
	v_sub_u32_e32 v5, v5, v0
	v_min_u32_e32 v5, v5, v26
	v_lshl_add_u32 v5, v5, 2, v27
	ds_add_u32 v5, v232
	v_lshrrev_b32_e32 v5, s33, v65
	v_sub_u32_e32 v5, v5, v0
	v_min_u32_e32 v5, v5, v26
	v_lshl_add_u32 v5, v5, 2, v27
	ds_add_u32 v5, v232
	v_lshrrev_b32_e32 v5, s33, v64
	v_sub_u32_e32 v5, v5, v0
	v_min_u32_e32 v5, v5, v26
	v_lshl_add_u32 v5, v5, 2, v27
	ds_add_u32 v5, v232
	v_lshrrev_b32_e32 v5, s33, v57
	v_sub_u32_e32 v5, v5, v0
	v_min_u32_e32 v5, v5, v26
	v_lshl_add_u32 v5, v5, 2, v27
	ds_add_u32 v5, v232
	v_lshrrev_b32_e32 v5, s33, v56
	v_sub_u32_e32 v5, v5, v0
	v_min_u32_e32 v5, v5, v26
	v_lshl_add_u32 v5, v5, 2, v27
	ds_add_u32 v5, v232
	v_lshrrev_b32_e32 v5, s33, v49
	v_sub_u32_e32 v5, v5, v0
	v_min_u32_e32 v5, v5, v26
	v_lshl_add_u32 v5, v5, 2, v27
	ds_add_u32 v5, v232
	v_lshrrev_b32_e32 v5, s33, v48
	v_sub_u32_e32 v5, v5, v0
	v_min_u32_e32 v5, v5, v26
	v_lshl_add_u32 v5, v5, 2, v27
	ds_add_u32 v5, v232
	v_lshrrev_b32_e32 v5, s33, v41
	v_sub_u32_e32 v5, v5, v0
	v_min_u32_e32 v5, v5, v26
	v_lshl_add_u32 v5, v5, 2, v27
	ds_add_u32 v5, v232
	v_lshrrev_b32_e32 v5, s33, v40
	v_sub_u32_e32 v5, v5, v0
	v_min_u32_e32 v5, v5, v26
	v_lshl_add_u32 v5, v5, 2, v27
	ds_add_u32 v5, v232
	v_lshrrev_b32_e32 v5, s33, v33
	v_sub_u32_e32 v5, v5, v0
	v_min_u32_e32 v5, v5, v26
	v_lshl_add_u32 v5, v5, 2, v27
	ds_add_u32 v5, v232
	v_lshrrev_b32_e32 v5, s33, v32
	v_sub_u32_e32 v5, v5, v0
	v_min_u32_e32 v5, v5, v26
	v_lshl_add_u32 v5, v5, 2, v27
	ds_add_u32 v5, v232
	v_lshrrev_b32_e32 v5, s33, v25
	v_sub_u32_e32 v5, v5, v0
	v_min_u32_e32 v5, v5, v26
	v_lshl_add_u32 v5, v5, 2, v27
	ds_add_u32 v5, v232
	v_lshrrev_b32_e32 v5, s33, v24
	v_sub_u32_e32 v5, v5, v0
	v_min_u32_e32 v5, v5, v26
	v_lshl_add_u32 v5, v5, 2, v27
	ds_add_u32 v5, v232
	v_lshrrev_b32_e32 v5, s33, v21
	v_sub_u32_e32 v5, v5, v0
	v_min_u32_e32 v5, v5, v26
	v_lshl_add_u32 v5, v5, 2, v27
	ds_add_u32 v5, v232
	v_lshrrev_b32_e32 v5, s33, v20
	v_sub_u32_e32 v5, v5, v0
	v_min_u32_e32 v5, v5, v26
	v_lshl_add_u32 v5, v5, 2, v27
	ds_add_u32 v5, v232

.LBB0_1040:
	v_lshrrev_b32_e32 v5, s33, v110
	v_sub_u32_e32 v5, v5, v0
	v_min_u32_e32 v5, v5, v26
	v_lshl_add_u32 v5, v5, 2, v27
	ds_add_u32 v5, v232
	v_lshrrev_b32_e32 v5, s33, v109
	v_sub_u32_e32 v5, v5, v0
	v_min_u32_e32 v5, v5, v26
	v_lshl_add_u32 v5, v5, 2, v27
	ds_add_u32 v5, v232
	v_lshrrev_b32_e32 v5, s33, v112
	v_sub_u32_e32 v5, v5, v0
	v_min_u32_e32 v5, v5, v26
	v_lshl_add_u32 v5, v5, 2, v27
	ds_add_u32 v5, v232
	v_lshrrev_b32_e32 v5, s33, v111
	v_sub_u32_e32 v5, v5, v0
	v_min_u32_e32 v5, v5, v26
	v_lshl_add_u32 v5, v5, 2, v27
	ds_add_u32 v5, v232
	v_lshrrev_b32_e32 v5, s33, v114
	v_sub_u32_e32 v5, v5, v0
	v_min_u32_e32 v5, v5, v26
	v_lshl_add_u32 v5, v5, 2, v27
	ds_add_u32 v5, v232
	v_lshrrev_b32_e32 v5, s33, v113
	v_sub_u32_e32 v5, v5, v0
	v_min_u32_e32 v5, v5, v26
	v_lshl_add_u32 v5, v5, 2, v27
	ds_add_u32 v5, v232
	v_lshrrev_b32_e32 v5, s33, v116
	v_sub_u32_e32 v5, v5, v0
	v_min_u32_e32 v5, v5, v26
	v_lshl_add_u32 v5, v5, 2, v27
	ds_add_u32 v5, v232
	v_lshrrev_b32_e32 v5, s33, v115
	v_sub_u32_e32 v5, v5, v0
	v_min_u32_e32 v5, v5, v26
	v_lshl_add_u32 v5, v5, 2, v27
	ds_add_u32 v5, v232
	v_lshrrev_b32_e32 v5, s33, v118
	v_sub_u32_e32 v5, v5, v0
	v_min_u32_e32 v5, v5, v26
	v_lshl_add_u32 v5, v5, 2, v27
	ds_add_u32 v5, v232
	v_lshrrev_b32_e32 v5, s33, v117
	v_sub_u32_e32 v5, v5, v0
	v_min_u32_e32 v5, v5, v26
	v_lshl_add_u32 v5, v5, 2, v27
	ds_add_u32 v5, v232
	v_lshrrev_b32_e32 v5, s33, v120
	v_sub_u32_e32 v5, v5, v0
	v_min_u32_e32 v5, v5, v26
	v_lshl_add_u32 v5, v5, 2, v27
	ds_add_u32 v5, v232
	v_lshrrev_b32_e32 v5, s33, v119
	v_sub_u32_e32 v5, v5, v0
	v_min_u32_e32 v5, v5, v26
	v_lshl_add_u32 v5, v5, 2, v27
	ds_add_u32 v5, v232
	v_lshrrev_b32_e32 v5, s33, v122
	v_sub_u32_e32 v5, v5, v0
	v_min_u32_e32 v5, v5, v26
	v_lshl_add_u32 v5, v5, 2, v27
	ds_add_u32 v5, v232
	v_lshrrev_b32_e32 v5, s33, v121
	v_sub_u32_e32 v5, v5, v0
	v_min_u32_e32 v5, v5, v26
	v_lshl_add_u32 v5, v5, 2, v27
	ds_add_u32 v5, v232
	v_lshrrev_b32_e32 v5, s33, v124
	v_sub_u32_e32 v5, v5, v0
	v_min_u32_e32 v5, v5, v26
	v_lshl_add_u32 v5, v5, 2, v27
	ds_add_u32 v5, v232
	v_lshrrev_b32_e32 v5, s33, v123
	v_sub_u32_e32 v5, v5, v0
	v_min_u32_e32 v5, v5, v26
	v_lshl_add_u32 v5, v5, 2, v27
	ds_add_u32 v5, v232
	s_andn2_b64 vcc, exec, s[6:7]
	s_cbranch_vccz .LBB0_976

.LBB0_1042:
	v_lshrrev_b32_e32 v5, s33, v142
	v_sub_u32_e32 v5, v5, v0
	v_min_u32_e32 v5, v5, v26
	v_lshl_add_u32 v5, v5, 2, v27
	ds_add_u32 v5, v232
	v_lshrrev_b32_e32 v5, s33, v141
	v_sub_u32_e32 v5, v5, v0
	v_min_u32_e32 v5, v5, v26
	v_lshl_add_u32 v5, v5, 2, v27
	ds_add_u32 v5, v232
	v_lshrrev_b32_e32 v5, s33, v144
	v_sub_u32_e32 v5, v5, v0
	v_min_u32_e32 v5, v5, v26
	v_lshl_add_u32 v5, v5, 2, v27
	ds_add_u32 v5, v232
	v_lshrrev_b32_e32 v5, s33, v143
	v_sub_u32_e32 v5, v5, v0
	v_min_u32_e32 v5, v5, v26
	v_lshl_add_u32 v5, v5, 2, v27
	ds_add_u32 v5, v232
	v_lshrrev_b32_e32 v5, s33, v146
	v_sub_u32_e32 v5, v5, v0
	v_min_u32_e32 v5, v5, v26
	v_lshl_add_u32 v5, v5, 2, v27
	ds_add_u32 v5, v232
	v_lshrrev_b32_e32 v5, s33, v145
	v_sub_u32_e32 v5, v5, v0
	v_min_u32_e32 v5, v5, v26
	v_lshl_add_u32 v5, v5, 2, v27
	ds_add_u32 v5, v232
	v_lshrrev_b32_e32 v5, s33, v148
	v_sub_u32_e32 v5, v5, v0
	v_min_u32_e32 v5, v5, v26
	v_lshl_add_u32 v5, v5, 2, v27
	ds_add_u32 v5, v232
	v_lshrrev_b32_e32 v5, s33, v147
	v_sub_u32_e32 v5, v5, v0
	v_min_u32_e32 v5, v5, v26
	v_lshl_add_u32 v5, v5, 2, v27
	ds_add_u32 v5, v232
	v_lshrrev_b32_e32 v5, s33, v150
	v_sub_u32_e32 v5, v5, v0
	v_min_u32_e32 v5, v5, v26
	v_lshl_add_u32 v5, v5, 2, v27
	ds_add_u32 v5, v232
	v_lshrrev_b32_e32 v5, s33, v149
	v_sub_u32_e32 v5, v5, v0
	v_min_u32_e32 v5, v5, v26
	v_lshl_add_u32 v5, v5, 2, v27
	ds_add_u32 v5, v232
	v_lshrrev_b32_e32 v5, s33, v152
	v_sub_u32_e32 v5, v5, v0
	v_min_u32_e32 v5, v5, v26
	v_lshl_add_u32 v5, v5, 2, v27
	ds_add_u32 v5, v232
	v_lshrrev_b32_e32 v5, s33, v151
	v_sub_u32_e32 v5, v5, v0
	v_min_u32_e32 v5, v5, v26
	v_lshl_add_u32 v5, v5, 2, v27
	ds_add_u32 v5, v232
	v_lshrrev_b32_e32 v5, s33, v154
	v_sub_u32_e32 v5, v5, v0
	v_min_u32_e32 v5, v5, v26
	v_lshl_add_u32 v5, v5, 2, v27
	ds_add_u32 v5, v232
	v_lshrrev_b32_e32 v5, s33, v153
	v_sub_u32_e32 v5, v5, v0
	v_min_u32_e32 v5, v5, v26
	v_lshl_add_u32 v5, v5, 2, v27
	ds_add_u32 v5, v232
	v_lshrrev_b32_e32 v5, s33, v156
	v_sub_u32_e32 v5, v5, v0
	v_min_u32_e32 v5, v5, v26
	v_lshl_add_u32 v5, v5, 2, v27
	ds_add_u32 v5, v232
	v_lshrrev_b32_e32 v5, s33, v155
	v_sub_u32_e32 v5, v5, v0
	v_min_u32_e32 v5, v5, v26
	v_lshl_add_u32 v5, v5, 2, v27
	ds_add_u32 v5, v232
	s_andn2_b64 vcc, exec, s[72:73]
	s_cbranch_vccz .LBB0_978

.LBB0_1044:
	v_lshrrev_b32_e32 v5, s33, v174
	v_sub_u32_e32 v5, v5, v0
	v_min_u32_e32 v5, v5, v26
	v_lshl_add_u32 v5, v5, 2, v27
	ds_add_u32 v5, v232
	v_lshrrev_b32_e32 v5, s33, v173
	v_sub_u32_e32 v5, v5, v0
	v_min_u32_e32 v5, v5, v26
	v_lshl_add_u32 v5, v5, 2, v27
	ds_add_u32 v5, v232
	v_lshrrev_b32_e32 v5, s33, v176
	v_sub_u32_e32 v5, v5, v0
	v_min_u32_e32 v5, v5, v26
	v_lshl_add_u32 v5, v5, 2, v27
	ds_add_u32 v5, v232
	v_lshrrev_b32_e32 v5, s33, v175
	v_sub_u32_e32 v5, v5, v0
	v_min_u32_e32 v5, v5, v26
	v_lshl_add_u32 v5, v5, 2, v27
	ds_add_u32 v5, v232
	v_lshrrev_b32_e32 v5, s33, v178
	v_sub_u32_e32 v5, v5, v0
	v_min_u32_e32 v5, v5, v26
	v_lshl_add_u32 v5, v5, 2, v27
	ds_add_u32 v5, v232
	v_lshrrev_b32_e32 v5, s33, v177
	v_sub_u32_e32 v5, v5, v0
	v_min_u32_e32 v5, v5, v26
	v_lshl_add_u32 v5, v5, 2, v27
	ds_add_u32 v5, v232
	v_lshrrev_b32_e32 v5, s33, v180
	v_sub_u32_e32 v5, v5, v0
	v_min_u32_e32 v5, v5, v26
	v_lshl_add_u32 v5, v5, 2, v27
	ds_add_u32 v5, v232
	v_lshrrev_b32_e32 v5, s33, v179
	v_sub_u32_e32 v5, v5, v0
	v_min_u32_e32 v5, v5, v26
	v_lshl_add_u32 v5, v5, 2, v27
	ds_add_u32 v5, v232
	v_lshrrev_b32_e32 v5, s33, v182
	v_sub_u32_e32 v5, v5, v0
	v_min_u32_e32 v5, v5, v26
	v_lshl_add_u32 v5, v5, 2, v27
	ds_add_u32 v5, v232
	v_lshrrev_b32_e32 v5, s33, v181
	v_sub_u32_e32 v5, v5, v0
	v_min_u32_e32 v5, v5, v26
	v_lshl_add_u32 v5, v5, 2, v27
	ds_add_u32 v5, v232
	v_lshrrev_b32_e32 v5, s33, v184
	v_sub_u32_e32 v5, v5, v0
	v_min_u32_e32 v5, v5, v26
	v_lshl_add_u32 v5, v5, 2, v27
	ds_add_u32 v5, v232
	v_lshrrev_b32_e32 v5, s33, v183
	v_sub_u32_e32 v5, v5, v0
	v_min_u32_e32 v5, v5, v26
	v_lshl_add_u32 v5, v5, 2, v27
	ds_add_u32 v5, v232
	v_lshrrev_b32_e32 v5, s33, v186
	v_sub_u32_e32 v5, v5, v0
	v_min_u32_e32 v5, v5, v26
	v_lshl_add_u32 v5, v5, 2, v27
	ds_add_u32 v5, v232
	v_lshrrev_b32_e32 v5, s33, v185
	v_sub_u32_e32 v5, v5, v0
	v_min_u32_e32 v5, v5, v26
	v_lshl_add_u32 v5, v5, 2, v27
	ds_add_u32 v5, v232
	v_lshrrev_b32_e32 v5, s33, v188
	v_sub_u32_e32 v5, v5, v0
	v_min_u32_e32 v5, v5, v26
	v_lshl_add_u32 v5, v5, 2, v27
	ds_add_u32 v5, v232
	v_lshrrev_b32_e32 v5, s33, v187
	v_sub_u32_e32 v5, v5, v0
	v_min_u32_e32 v5, v5, v26
	v_lshl_add_u32 v5, v5, 2, v27
	ds_add_u32 v5, v232
	s_andn2_b64 vcc, exec, s[62:63]
	s_cbranch_vccz .LBB0_980
	s_branch .LBB0_981
